# v4 bundle + MLA attention: tile-0/1 K/V DMAs issued before the q rows are loaded and finished
# speedup vs baseline: 1.0029x; 1.0029x over previous
; #define LAS __attribute__((address_space(3)))
; __device__ __forceinline__ int v_rd_base(int lane) { return ((lane & 3) << 3) | (((lane >> 2) & 3) << 6) | (((lane >> 4) & 1) << 5) | (((lane >> 5) & 1) << 8); }
; __device__ __forceinline__ float half_pair_sum(float v) { const unsigned a = __float_as_uint(v); auto rr = __builtin_amdgcn_permlane32_swap(a, a, false, false); const unsigned r0 = rr[0], r1 = rr[1]; return __uint_as_float(r0) + __uint_as_float(r1); }
; #define DMA_WAIT(last) do { if (last) asm volatile("s_waitcnt vmcnt(0)" ::: "memory"); else asm volatile("s_waitcnt vmcnt(%0)" :: "n"(NPW) : "memory"); } while (0)
;   __device__ __forceinline__ void load(bf16x8 (&qr)[6], int r, int hi) const {
;     const bf16* src = qpre + (long)r * 1536 + hi * 8; float v[6][8]; float ss = 0.f;
; #pragma unroll
;     for (int d0 = 0; d0 < 6; ++d0) { unpack_bf8(*reinterpret_cast<const bf16x8*>(src + d0 * 16), v[d0]);
; #pragma unroll
;       for (int j = 0; j < 8; ++j) ss += v[d0][j] * v[d0][j]; }
;     ss = half_pair_sum(ss);
;     const float rqv = rq[r], f = Sc<96>::C * rqv / sqrtf(rqv * rqv * ss * (1.0f / 96.0f) + EPS);
; template <int DK, int DV, bool OFF, class QLoader> ...
;     ...
;   unsigned koff[KPW], voff[VPW];
; #pragma unroll
;   for (int i = 0; i < (DK == 64 ? 1 : KPW); ++i) { const int row = (wid * KPW + i) * 4 + (lane >> 4); int c = (lane & 15) ^ (row & 7); c = (c < DK / 8) ? c : (c & 7); koff[i] = (unsigned)((row * ldk) * 2 + c * 16); }
; #pragma unroll
;   for (int i = 0; i < 1; ++i) { const int sidx = (wid * VPW + i) * 2 + (lane >> 5), kg = sidx / ND, st = sidx % ND, kk = kg * 8 + ((lane & 31) >> 2);
;     const int k = (kk & ~0xC) | ((kk & 4) << 1) | ((kk & 8) >> 1), c = st * 32 + (lane & 3) * 8; voff[i] = (unsigned)((k * ldv + c) * 2); }
;   const int vb0 = (int)(uintptr_t)V_lds + v_rd_base(lane);
;   LAS unsigned* const ldsK = (LAS unsigned*)(LAS char*)K_lds + (wid * KPW) * 256; LAS unsigned* const ldsV = (LAS unsigned*)(LAS char*)V_lds + (wid * VPW) * 256;
;     ...
;   f32x16 pA0, pA1, pB0, pB1; bf16x8 pa0, pa1, pa2, pa3; const int NT = nkeys / KVBLK;
;   DMA_TILE(0, 0); DMA_TILE(1, 1); DMA_WAIT(false); __syncthreads(); if (2 < NT) DMA_TILE(2, 2);
.LBB0_1412:
	s_and_b32 s30, s22, 15
	s_ashr_i32 s1, s0, 31
	s_mul_i32 s17, s0, 0xc00
	s_mul_hi_i32 s16, s0, 0xc00
	s_add_u32 s17, s63, s17
	s_addc_u32 s16, s64, s16
	s_mul_i32 s20, s30, 0xc0
	s_add_u32 s28, s17, s20
	s_addc_u32 s29, s16, 0
	s_lshl_b64 s[16:17], s[0:1], 2
	s_add_u32 s26, s72, s16
	s_addc_u32 s27, s73, s17
	s_lshl_b32 s2, s2, 14
	s_add_u32 s24, s69, s2
	s_addc_u32 s25, s70, 0
	s_mul_i32 s78, s22, 0xcc000
	s_mul_hi_i32 s2, s22, 0xcc000
	s_add_u32 s20, s65, s78
	s_addc_u32 s21, s66, s2
	s_mul_i32 s80, s22, 0x88000
	s_mul_hi_i32 s79, s22, 0x88000
	s_add_u32 s22, s74, s80
	s_addc_u32 s23, s75, s79
	s_lshl_b64 s[0:1], s[0:1], 11
	s_add_u32 s0, s67, s0
	s_addc_u32 s1, s68, s1
	s_lshl_b32 s16, s30, 7
	s_add_u32 s16, s0, s16
	v_cndmask_b32_e64 v0, 0, 1, s[18:19]
	s_addc_u32 s17, s1, 0
	s_mov_b64 s[0:1], -1
	s_andn2_b64 vcc, exec, s[34:35]
	v_cmp_ne_u32_e64 s[36:37], 1, v0
	s_cbranch_vccnz .LBB0_1463
	v_mov_b32_e32 v56, v180
	v_mov_b64_e32 v[2:3], s[28:29]
	v_readfirstlane_b32 s31, v56
	s_ashr_i32 s38, s31, 6
	v_and_b32_e32 v55, 31, v56
	s_lshl_b32 s30, s38, 5
	v_bfe_u32 v57, v56, 5, 1
	v_or_b32_e32 v36, s30, v55
	s_movk_i32 s0, 0xc00
	v_mad_i64_i32 v[2:3], s[0:1], v36, s0, v[2:3]
	v_lshlrev_b32_e32 v34, 4, v57
	v_mov_b32_e32 v35, v1
	v_lshl_add_u64 v[2:3], v[2:3], 0, v[34:35]
	v_bfe_u32 v188, v56, 4, 2
	v_lshl_or_b32 v189, s38, 3, v188
	v_bitop3_b32 v193, v188, v56, 15 bitop3:0x78
	s_movk_i32 s0, 0xc0
	v_and_b32_e32 v192, 15, v56
	v_mul_lo_u32 v194, v189, s0
	v_lshlrev_b32_e32 v189, 4, v193
	v_and_b32_e32 v193, 0x70, v189
	v_cmp_gt_u32_e32 vcc, 12, v192
	v_bitop3_b32 v192, v188, v192, 4 bitop3:0x36
	v_lshl_or_b32 v199, s38, 1, v57
	v_cndmask_b32_e32 v197, v193, v189, vcc
	v_lshlrev_b32_e32 v193, 4, v192
	v_cmp_gt_u32_e32 vcc, 12, v192
	v_lshrrev_b32_e32 v192, 31, v199
	v_and_b32_e32 v195, 0x70, v193
	v_add_u32_e32 v192, v199, v192
	v_cndmask_b32_e32 v196, v195, v193, vcc
	s_movk_i32 s0, 0x300
	v_ashrrev_i32_e32 v198, 1, v192
	v_add_u32_e32 v189, v197, v194
	v_add3_u32 v204, v194, v196, s0
	v_lshlrev_b32_e32 v193, 3, v198
	v_lshrrev_b32_e32 v194, 2, v55
	s_mov_b32 s0, 0x1fffff3
	v_bitop3_b32 v200, v193, s0, v194 bitop3:0xc8
	s_lshl_b32 s0, s38, 11
	v_lshrrev_b32_e32 v193, 1, v55
	s_add_i32 s87, s0, 0
	v_and_b32_e32 v192, 0x3fffffe, v192
	v_and_b32_e32 v201, 8, v193
	v_lshlrev_b32_e32 v193, 2, v198
	v_lshlrev_b32_e32 v194, 4, v56
	s_add_i32 s81, s87, 0x8000
	s_lshl_b32 s1, s38, 10
	v_sub_u32_e32 v192, v199, v192
	v_and_b32_e32 v202, 4, v193
	v_and_b32_e32 v203, 48, v194
	s_sub_i32 s0, 0, s1
	s_sub_i32 s1, s87, s1
	s_mov_b32 m0, s81
	s_add_i32 s82, s87, 0x8400
	v_or3_b32 v193, v201, v200, v202
	v_lshl_or_b32 v192, v192, 6, v203
	global_load_lds_dwordx4 v189, s[20:21]
	s_mov_b32 m0, s82
	s_add_u32 s40, s20, 0x3000
	v_lshl_add_u32 v192, v193, 7, v192
	global_load_lds_dwordx4 v204, s[20:21]
	s_mov_b32 m0, s1
	s_addc_u32 s41, s21, 0
	s_add_i32 s83, s87, 0xc000
	global_load_lds_dwordx4 v192, s[22:23]
	s_mov_b32 m0, s83
	s_add_i32 s84, s87, 0xc400
	v_mov_b32_e32 v193, v1
	global_load_lds_dwordx4 v189, s[40:41]
	s_mov_b32 m0, s84
	v_lshl_add_u64 v[206:207], s[22:23], 0, v[192:193]
	global_load_lds_dwordx4 v204, s[40:41]
	s_mov_b64 s[40:41], 0x2000
	s_add_i32 m0, s1, 0x2000
	v_lshl_add_u64 v[192:193], v[206:207], 0, s[40:41]
	s_add_u32 s40, s20, 0x6000
	global_load_lds_dwordx4 v[192:193], off
	global_load_dwordx4 v[38:41], v[2:3], off
	global_load_dwordx4 v[42:45], v[2:3], off offset:32
	global_load_dwordx4 v[46:49], v[2:3], off offset:64
	global_load_dwordx4 v[50:53], v[2:3], off offset:96
	v_ashrrev_i32_e32 v37, 31, v36
	v_lshl_add_u64 v[4:5], v[36:37], 2, s[26:27]
	global_load_dword v0, v[4:5], off
	global_load_dwordx4 v[90:93], v[2:3], off offset:128
	global_load_dwordx4 v[94:97], v[2:3], off offset:160
	v_and_b32_e32 v35, 32, v56
	global_load_dwordx4 v[6:9], v35, s[14:15] offset:16
	global_load_dwordx4 v[2:5], v35, s[14:15]
	global_load_dwordx4 v[14:17], v35, s[14:15] offset:80
	global_load_dwordx4 v[10:13], v35, s[14:15] offset:64
	global_load_dwordx4 v[22:25], v35, s[14:15] offset:144
	global_load_dwordx4 v[18:21], v35, s[14:15] offset:128
	global_load_dwordx4 v[30:33], v35, s[14:15] offset:208
	global_load_dwordx4 v[26:29], v35, s[14:15] offset:192
	global_load_dwordx4 v[98:101], v35, s[14:15] offset:256
	global_load_dwordx4 v[102:105], v35, s[14:15] offset:272
	global_load_dwordx4 v[106:109], v35, s[14:15] offset:320
	global_load_dwordx4 v[110:113], v35, s[14:15] offset:336
	s_mov_b32 s0, 0xf800000
	s_waitcnt vmcnt(18)
	v_and_b32_e32 v58, 0xffff0000, v38
	v_lshlrev_b32_e32 v35, 16, v38
	v_mul_f32_e32 v89, v58, v58
	v_lshlrev_b32_e32 v60, 16, v39
	v_fmac_f32_e32 v89, v35, v35
	v_and_b32_e32 v62, 0xffff0000, v39
	v_fmac_f32_e32 v89, v60, v60
	v_lshlrev_b32_e32 v59, 16, v40
	v_fmac_f32_e32 v89, v62, v62
	v_and_b32_e32 v61, 0xffff0000, v40
	v_fmac_f32_e32 v89, v59, v59
	v_lshlrev_b32_e32 v63, 16, v41
	v_fmac_f32_e32 v89, v61, v61
	v_and_b32_e32 v64, 0xffff0000, v41
	v_fmac_f32_e32 v89, v63, v63
	s_waitcnt vmcnt(17)
	v_lshlrev_b32_e32 v65, 16, v42
	v_fmac_f32_e32 v89, v64, v64
	v_and_b32_e32 v66, 0xffff0000, v42
	v_fmac_f32_e32 v89, v65, v65
	v_lshlrev_b32_e32 v68, 16, v43
	v_fmac_f32_e32 v89, v66, v66
	v_and_b32_e32 v70, 0xffff0000, v43
	v_fmac_f32_e32 v89, v68, v68
	v_lshlrev_b32_e32 v67, 16, v44
	v_fmac_f32_e32 v89, v70, v70
	v_and_b32_e32 v69, 0xffff0000, v44
	v_fmac_f32_e32 v89, v67, v67
	v_lshlrev_b32_e32 v71, 16, v45
	v_fmac_f32_e32 v89, v69, v69
	v_and_b32_e32 v72, 0xffff0000, v45
	v_fmac_f32_e32 v89, v71, v71
	s_waitcnt vmcnt(16)
; __device__ __forceinline__ float half_pair_sum(float v) { const unsigned a = __float_as_uint(v); auto rr = __builtin_amdgcn_permlane32_swap(a, a, false, false); const unsigned r0 = rr[0], r1 = rr[1]; return __uint_as_float(r0) + __uint_as_float(r1); }
;   __device__ __forceinline__ void load(bf16x8 (&qr)[6], int r, int hi) const {
;     const bf16* src = qpre + (long)r * 1536 + hi * 8; float v[6][8]; float ss = 0.f;
; #pragma unroll
;     for (int d0 = 0; d0 < 6; ++d0) { unpack_bf8(*reinterpret_cast<const bf16x8*>(src + d0 * 16), v[d0]);
; #pragma unroll
;       for (int j = 0; j < 8; ++j) ss += v[d0][j] * v[d0][j]; }
;     ss = half_pair_sum(ss);
;     const float rqv = rq[r], f = Sc<96>::C * rqv / sqrtf(rqv * rqv * ss * (1.0f / 96.0f) + EPS);
; #pragma unroll
;     for (int d0 = 0; d0 < 6; ++d0) { const f32x4 g0 = *(const f32x4*)(gq + d0 * 16 + hi * 8), g1 = *(const f32x4*)(gq + d0 * 16 + hi * 8 + 4);
; #pragma unroll
;       for (int j = 0; j < 4; ++j) { v[d0][j] *= f * g0[j]; v[d0][4 + j] *= f * g1[j]; } }
;     if (cosA) { const float* c = cosA + (long)r * 16 + hi * 8; const float* sn = c + 4096 * 16;
; #pragma unroll
;       for (int j = 0; j < 8; ++j) { const float x1 = v[4][j], x2 = v[5][j], cs = c[j], si = sn[j]; v[4][j] = x1 * cs - x2 * si; v[5][j] = x1 * si + x2 * cs; } }
	v_lshlrev_b32_e32 v73, 16, v46
	v_fmac_f32_e32 v89, v72, v72
	v_and_b32_e32 v74, 0xffff0000, v46
	v_fmac_f32_e32 v89, v73, v73
	v_lshlrev_b32_e32 v76, 16, v47
	v_fmac_f32_e32 v89, v74, v74
	v_and_b32_e32 v78, 0xffff0000, v47
	v_fmac_f32_e32 v89, v76, v76
	v_lshlrev_b32_e32 v75, 16, v48
	v_fmac_f32_e32 v89, v78, v78
	v_and_b32_e32 v77, 0xffff0000, v48
	v_fmac_f32_e32 v89, v75, v75
	v_lshlrev_b32_e32 v79, 16, v49
	v_fmac_f32_e32 v89, v77, v77
	v_and_b32_e32 v80, 0xffff0000, v49
	v_fmac_f32_e32 v89, v79, v79
	s_waitcnt vmcnt(15)
	v_lshlrev_b32_e32 v81, 16, v50
	v_fmac_f32_e32 v89, v80, v80
	v_and_b32_e32 v82, 0xffff0000, v50
	v_fmac_f32_e32 v89, v81, v81
	v_lshlrev_b32_e32 v84, 16, v51
	v_fmac_f32_e32 v89, v82, v82
	v_and_b32_e32 v86, 0xffff0000, v51
	v_fmac_f32_e32 v89, v84, v84
	v_lshlrev_b32_e32 v83, 16, v52
	v_fmac_f32_e32 v89, v86, v86
	v_and_b32_e32 v85, 0xffff0000, v52
	v_fmac_f32_e32 v89, v83, v83
	v_lshlrev_b32_e32 v87, 16, v53
	v_fmac_f32_e32 v89, v85, v85
	v_and_b32_e32 v88, 0xffff0000, v53
	s_waitcnt vmcnt(13)
	v_and_b32_e32 v47, 0xffff0000, v90
	v_lshlrev_b32_e32 v46, 16, v90
	v_fmac_f32_e32 v89, v87, v87
	v_fmac_f32_e32 v89, v88, v88
	v_pk_mul_f32 v[118:119], v[46:47], v[46:47]
	v_and_b32_e32 v45, 0xffff0000, v91
	v_lshlrev_b32_e32 v44, 16, v91
	v_add_f32_e32 v89, v118, v89
	v_pk_mul_f32 v[114:115], v[44:45], v[44:45]
	v_add_f32_e32 v89, v119, v89
	v_and_b32_e32 v41, 0xffff0000, v92
	v_lshlrev_b32_e32 v40, 16, v92
	v_add_f32_e32 v89, v114, v89
	v_pk_mul_f32 v[90:91], v[40:41], v[40:41]
	v_add_f32_e32 v89, v115, v89
	v_and_b32_e32 v39, 0xffff0000, v93
	v_lshlrev_b32_e32 v38, 16, v93
	v_add_f32_e32 v89, v90, v89
	v_pk_mul_f32 v[50:51], v[38:39], v[38:39]
	v_add_f32_e32 v89, v91, v89
	s_waitcnt vmcnt(12)
	v_and_b32_e32 v93, 0xffff0000, v95
	v_lshlrev_b32_e32 v92, 16, v95
	v_and_b32_e32 v95, 0xffff0000, v94
	v_lshlrev_b32_e32 v94, 16, v94
	v_add_f32_e32 v50, v50, v89
	v_pk_mul_f32 v[118:119], v[94:95], v[94:95]
	v_add_f32_e32 v50, v51, v50
	v_add_f32_e32 v50, v118, v50
	v_pk_mul_f32 v[116:117], v[92:93], v[92:93]
	v_add_f32_e32 v50, v119, v50
	v_and_b32_e32 v49, 0xffff0000, v96
	v_lshlrev_b32_e32 v48, 16, v96
	v_add_f32_e32 v50, v116, v50
	v_and_b32_e32 v43, 0xffff0000, v97
	v_lshlrev_b32_e32 v42, 16, v97
	v_pk_mul_f32 v[96:97], v[48:49], v[48:49]
	v_add_f32_e32 v50, v117, v50
	v_add_f32_e32 v50, v96, v50
	v_pk_mul_f32 v[52:53], v[42:43], v[42:43]
	v_add_f32_e32 v50, v97, v50
	v_add_f32_e32 v50, v52, v50
	v_add_f32_e32 v50, v53, v50
	v_mov_b32_e32 v51, v50
	s_nop 1
	v_permlane32_swap_b32_e32 v50, v51
	v_mul_f32_e32 v54, v0, v0
	v_add_f32_e32 v50, v50, v51
	v_mul_f32_e32 v50, v54, v50
	v_fmamk_f32 v50, v50, 0x3c2aaaab, v250
	v_mul_f32_e32 v51, 0x4f800000, v50
	v_cmp_gt_f32_e32 vcc, s0, v50
	v_mul_f32_e32 v0, 0x3e16c740, v0
	s_nop 0
	v_cndmask_b32_e32 v50, v50, v51, vcc
	v_sqrt_f32_e32 v51, v50
	s_nop 0
	v_add_u32_e32 v52, -1, v51
	v_fma_f32 v53, -v52, v51, v50
	v_cmp_ge_f32_e64 s[0:1], 0, v53
	v_add_u32_e32 v53, 1, v51
	s_nop 0
	v_cndmask_b32_e64 v52, v51, v52, s[0:1]
	v_fma_f32 v51, -v53, v51, v50
	v_cmp_lt_f32_e64 s[0:1], 0, v51
	s_nop 1
	v_cndmask_b32_e64 v51, v52, v53, s[0:1]
	v_mul_f32_e32 v52, 0x37800000, v51
	v_cndmask_b32_e32 v51, v51, v52, vcc
	v_cmp_class_f32_e32 vcc, v50, v146
	s_nop 1
	v_cndmask_b32_e32 v50, v51, v50, vcc
	v_div_scale_f32 v51, s[0:1], v50, v50, v0
	v_rcp_f32_e32 v52, v51
	s_nop 0
	v_fma_f32 v53, -v51, v52, 1.0
	v_fmac_f32_e32 v52, v53, v52
	v_div_scale_f32 v53, vcc, v0, v50, v0
	v_mul_f32_e32 v54, v53, v52
	v_fma_f32 v89, -v51, v54, v53
	v_fmac_f32_e32 v54, v89, v52
	v_fma_f32 v51, -v51, v54, v53
	v_div_fmas_f32 v51, v51, v52, v54
	v_div_fixup_f32 v54, v51, v50, v0
	s_waitcnt vmcnt(3)
	v_pk_mul_f32 v[50:51], v[54:55], v[98:99] op_sel_hi:[0,1]
	s_waitcnt vmcnt(2)
	v_pk_mul_f32 v[52:53], v[54:55], v[102:103] op_sel_hi:[0,1]
	v_pk_mul_f32 v[50:51], v[50:51], v[46:47]
	v_pk_mul_f32 v[46:47], v[54:55], v[100:101] op_sel_hi:[0,1]
	v_pk_mul_f32 v[90:91], v[54:55], v[104:105] op_sel_hi:[0,1]
	v_pk_mul_f32 v[40:41], v[52:53], v[40:41]
	v_pk_mul_f32 v[52:53], v[46:47], v[44:45]
	v_pk_mul_f32 v[46:47], v[90:91], v[38:39]
	s_waitcnt vmcnt(1)
	v_pk_mul_f32 v[38:39], v[54:55], v[106:107] op_sel_hi:[0,1]
	s_waitcnt vmcnt(0)
	v_pk_mul_f32 v[90:91], v[54:55], v[110:111] op_sel_hi:[0,1]
	v_pk_mul_f32 v[44:45], v[38:39], v[94:95]
	v_pk_mul_f32 v[38:39], v[90:91], v[48:49]
	v_pk_mul_f32 v[48:49], v[54:55], v[108:109] op_sel_hi:[0,1]
	v_pk_mul_f32 v[90:91], v[54:55], v[112:113] op_sel_hi:[0,1]
	v_pk_mul_f32 v[48:49], v[48:49], v[92:93]
	s_and_b64 vcc, exec, s[36:37]
	v_pk_mul_f32 v[42:43], v[90:91], v[42:43]
	s_cbranch_vccnz .LBB0_1415
	v_lshlrev_b32_e32 v0, 3, v57
	v_lshlrev_b64 v[36:37], 6, v[36:37]
	v_lshl_add_u64 v[36:37], s[24:25], 0, v[36:37]
	v_lshlrev_b32_e32 v0, 2, v0
	v_lshl_add_u64 v[36:37], v[36:37], 0, v[0:1]
	s_mov_b64 s[0:1], 0x40000
	v_lshl_add_u64 v[102:103], v[36:37], 0, s[0:1]
	global_load_dwordx4 v[90:93], v[36:37], off offset:16
	global_load_dwordx4 v[94:97], v[36:37], off
	v_add_co_u32_e32 v36, vcc, 0x40000, v36
	s_nop 1
	v_addc_co_u32_e32 v37, vcc, 0, v37, vcc
	global_load_dwordx4 v[98:101], v[36:37], off
	s_nop 0
	global_load_dwordx4 v[102:105], v[102:103], off offset:16
	s_waitcnt vmcnt(1)
	v_pk_mul_f32 v[36:37], v[50:51], v[98:99]
	v_pk_mul_f32 v[98:99], v[44:45], v[98:99]
	v_pk_fma_f32 v[44:45], v[44:45], v[94:95], v[36:37]
	v_pk_fma_f32 v[50:51], v[50:51], v[94:95], v[98:99] neg_lo:[0,0,1] neg_hi:[0,0,1]
	v_pk_mul_f32 v[36:37], v[52:53], v[100:101]
	v_pk_mul_f32 v[94:95], v[48:49], v[100:101]
	v_pk_fma_f32 v[48:49], v[48:49], v[96:97], v[36:37]
	v_pk_fma_f32 v[52:53], v[52:53], v[96:97], v[94:95] neg_lo:[0,0,1] neg_hi:[0,0,1]
	s_waitcnt vmcnt(0)
	v_pk_mul_f32 v[36:37], v[40:41], v[102:103]
	v_pk_mul_f32 v[94:95], v[38:39], v[102:103]
	v_pk_fma_f32 v[38:39], v[38:39], v[90:91], v[36:37]
	v_pk_fma_f32 v[40:41], v[40:41], v[90:91], v[94:95] neg_lo:[0,0,1] neg_hi:[0,0,1]
	v_pk_mul_f32 v[36:37], v[46:47], v[104:105]
	v_pk_mul_f32 v[90:91], v[42:43], v[104:105]
	v_pk_fma_f32 v[42:43], v[42:43], v[92:93], v[36:37]
	v_pk_fma_f32 v[46:47], v[46:47], v[92:93], v[90:91] neg_lo:[0,0,1] neg_hi:[0,0,1]
; #define LAS __attribute__((address_space(3)))
; __device__ __forceinline__ int v_rd_base(int lane) { return ((lane & 3) << 3) | (((lane >> 2) & 3) << 6) | (((lane >> 4) & 1) << 5) | (((lane >> 5) & 1) << 8); }
; __device__ __forceinline__ bf16x8 pack_bf8(const float* f) { u32x4 w = {cvtpk(f[0], f[1]), cvtpk(f[2], f[3]), cvtpk(f[4], f[5]), cvtpk(f[6], f[7])}; return *reinterpret_cast<bf16x8*>(&w); }
; #define DMA_WAIT(last) do { if (last) asm volatile("s_waitcnt vmcnt(0)" ::: "memory"); else asm volatile("s_waitcnt vmcnt(%0)" :: "n"(NPW) : "memory"); } while (0)
;   __device__ __forceinline__ void load(bf16x8 (&qr)[6], int r, int hi) const {
;     ...
;     for (int d0 = 0; d0 < 6; ++d0) { const f32x4 g0 = *(const f32x4*)(gq + d0 * 16 + hi * 8), g1 = *(const f32x4*)(gq + d0 * 16 + hi * 8 + 4);
; #pragma unroll
;       for (int j = 0; j < 4; ++j) { v[d0][j] *= f * g0[j]; v[d0][4 + j] *= f * g1[j]; } }
;     if (cosA) { const float* c = cosA + (long)r * 16 + hi * 8; const float* sn = c + 4096 * 16;
; #pragma unroll
;       for (int j = 0; j < 8; ++j) { const float x1 = v[4][j], x2 = v[5][j], cs = c[j], si = sn[j]; v[4][j] = x1 * cs - x2 * si; v[5][j] = x1 * si + x2 * cs; } }
; #pragma unroll
;     for (int d0 = 0; d0 < 6; ++d0) qr[d0] = pack_bf8(v[d0]);
; template <int DK, int DV, bool OFF, class QLoader> ...
;     ...
;   unsigned koff[KPW], voff[VPW];
; #pragma unroll
;   for (int i = 0; i < (DK == 64 ? 1 : KPW); ++i) { const int row = (wid * KPW + i) * 4 + (lane >> 4); int c = (lane & 15) ^ (row & 7); c = (c < DK / 8) ? c : (c & 7); koff[i] = (unsigned)((row * ldk) * 2 + c * 16); }
; #pragma unroll
;   for (int i = 0; i < 1; ++i) { const int sidx = (wid * VPW + i) * 2 + (lane >> 5), kg = sidx / ND, st = sidx % ND, kk = kg * 8 + ((lane & 31) >> 2);
;     const int k = (kk & ~0xC) | ((kk & 4) << 1) | ((kk & 8) >> 1), c = st * 32 + (lane & 3) * 8; voff[i] = (unsigned)((k * ldv + c) * 2); }
;   const int vb0 = (int)(uintptr_t)V_lds + v_rd_base(lane);
;   LAS unsigned* const ldsK = (LAS unsigned*)(LAS char*)K_lds + (wid * KPW) * 256; LAS unsigned* const ldsV = (LAS unsigned*)(LAS char*)V_lds + (wid * VPW) * 256;
;     ...
;   f32x16 pA0, pA1, pB0, pB1; bf16x8 pa0, pa1, pa2, pa3; const int NT = nkeys / KVBLK;
;   DMA_TILE(0, 0); DMA_TILE(1, 1); DMA_WAIT(false); __syncthreads(); if (2 < NT) DMA_TILE(2, 2);
;   qkt<DK>(pA0, pA1, K_lds, qr, r32, hi); partialSM<DK, OFF>(pA0, pA1, negMC);
.LBB0_1415:
	v_and_b32_e32 v36, 63, v56
	v_mul_f32_e32 v0, v54, v33
	v_mul_f32_e32 v3, v3, v54
	v_mul_f32_e32 v0, v0, v88
	v_mul_f32_e32 v29, v54, v29
	v_mul_f32_e32 v32, v54, v32
	v_mul_f32_e32 v28, v54, v28
	v_mul_f32_e32 v31, v54, v31
	v_mul_f32_e32 v27, v54, v27
	v_mul_f32_e32 v30, v54, v30
	v_mul_f32_e32 v26, v54, v26
	v_mul_f32_e32 v25, v54, v25
	v_mul_f32_e32 v21, v21, v54
	v_mul_f32_e32 v24, v54, v24
	v_mul_f32_e32 v20, v20, v54
	v_mul_f32_e32 v23, v54, v23
	v_mul_f32_e32 v19, v19, v54
	v_mul_f32_e32 v22, v54, v22
	v_mul_f32_e32 v18, v18, v54
	v_mul_f32_e32 v17, v17, v54
	v_mul_f32_e32 v13, v13, v54
	v_mul_f32_e32 v16, v16, v54
	v_mul_f32_e32 v12, v12, v54
	v_mul_f32_e32 v15, v15, v54
	v_mul_f32_e32 v11, v11, v54
	v_mul_f32_e32 v14, v14, v54
	v_mul_f32_e32 v10, v10, v54
	v_mul_f32_e32 v9, v9, v54
	v_mul_f32_e32 v5, v5, v54
	v_mul_f32_e32 v8, v8, v54
	v_mul_f32_e32 v4, v4, v54
	v_mul_f32_e32 v7, v7, v54
	v_mul_f32_e32 v3, v3, v58
	v_mul_f32_e32 v6, v6, v54
	v_mul_f32_e32 v2, v2, v54
	v_lshrrev_b32_e32 v149, 4, v36
	v_mul_f32_e32 v29, v29, v86
	v_mul_f32_e32 v32, v32, v87
	v_mul_f32_e32 v28, v28, v84
	v_mul_f32_e32 v31, v31, v85
	v_mul_f32_e32 v27, v27, v82
	v_mul_f32_e32 v30, v30, v83
	v_mul_f32_e32 v26, v26, v81
	v_mul_f32_e32 v25, v25, v80
	v_mul_f32_e32 v21, v21, v78
	v_mul_f32_e32 v24, v24, v79
	v_mul_f32_e32 v20, v20, v76
	v_mul_f32_e32 v23, v23, v77
	v_mul_f32_e32 v19, v19, v74
	v_mul_f32_e32 v22, v22, v75
	v_mul_f32_e32 v18, v18, v73
	v_mul_f32_e32 v17, v17, v72
	v_mul_f32_e32 v13, v13, v70
	v_mul_f32_e32 v16, v16, v71
	v_mul_f32_e32 v12, v12, v68
	v_mul_f32_e32 v15, v15, v69
	v_mul_f32_e32 v11, v11, v66
	v_mul_f32_e32 v14, v14, v67
	v_mul_f32_e32 v10, v10, v65
	v_mul_f32_e32 v9, v9, v64
	v_mul_f32_e32 v5, v5, v62
	v_mul_f32_e32 v8, v8, v63
	v_mul_f32_e32 v4, v4, v60
	v_mul_f32_e32 v7, v7, v61
	v_mul_f32_e32 v6, v6, v59
	v_mul_f32_e32 v2, v2, v35
	v_cvt_pk_bf16_f32 v98, v2, v3
	v_cvt_pk_bf16_f32 v99, v4, v5
	v_cvt_pk_bf16_f32 v100, v6, v7
	v_cvt_pk_bf16_f32 v101, v8, v9
	v_cvt_pk_bf16_f32 v102, v10, v11
	v_cvt_pk_bf16_f32 v103, v12, v13
	v_cvt_pk_bf16_f32 v104, v14, v15
	v_cvt_pk_bf16_f32 v105, v16, v17
	v_cvt_pk_bf16_f32 v106, v18, v19
	v_cvt_pk_bf16_f32 v107, v20, v21
	v_cvt_pk_bf16_f32 v108, v22, v23
	v_cvt_pk_bf16_f32 v109, v24, v25
	v_cvt_pk_bf16_f32 v110, v26, v27
	v_cvt_pk_bf16_f32 v111, v28, v29
	v_cvt_pk_bf16_f32 v112, v30, v31
	v_cvt_pk_bf16_f32 v113, v32, v0
	v_lshl_or_b32 v0, s38, 3, v149
	v_bitop3_b32 v3, v149, v56, 15 bitop3:0x78
	s_movk_i32 s0, 0xc0
	v_and_b32_e32 v2, 15, v56
	v_mul_lo_u32 v4, v0, s0
	v_lshlrev_b32_e32 v0, 4, v3
	v_and_b32_e32 v3, 0x70, v0
	v_cmp_gt_u32_e32 vcc, 12, v2
	v_bitop3_b32 v2, v149, v2, 4 bitop3:0x36
	v_lshl_or_b32 v153, s38, 1, v57
	v_cndmask_b32_e32 v151, v3, v0, vcc
	v_lshlrev_b32_e32 v3, 4, v2
	v_cmp_gt_u32_e32 vcc, 12, v2
	v_lshrrev_b32_e32 v2, 31, v153
	v_and_b32_e32 v5, 0x70, v3
	v_add_u32_e32 v2, v153, v2
	v_cndmask_b32_e32 v150, v5, v3, vcc
	s_movk_i32 s0, 0x300
	v_ashrrev_i32_e32 v152, 1, v2
	v_add_u32_e32 v0, v151, v4
	v_add3_u32 v122, v4, v150, s0
	v_lshlrev_b32_e32 v3, 3, v152
	v_lshrrev_b32_e32 v4, 2, v55
	s_mov_b32 s0, 0x1fffff3
	v_bitop3_b32 v154, v3, s0, v4 bitop3:0xc8
	s_lshl_b32 s0, s38, 11
	v_lshrrev_b32_e32 v3, 1, v55
	s_add_i32 s87, s0, 0
	v_and_b32_e32 v2, 0x3fffffe, v2
	v_and_b32_e32 v155, 8, v3
	v_lshlrev_b32_e32 v3, 2, v152
	v_lshlrev_b32_e32 v4, 4, v56
	s_add_i32 s81, s87, 0x8000
	s_lshl_b32 s1, s38, 10
	v_cvt_pk_bf16_f32 v114, v50, v51
	v_cvt_pk_bf16_f32 v115, v52, v53
	v_cvt_pk_bf16_f32 v116, v40, v41
	v_cvt_pk_bf16_f32 v117, v46, v47
	v_cvt_pk_bf16_f32 v118, v44, v45
	v_cvt_pk_bf16_f32 v119, v48, v49
	v_cvt_pk_bf16_f32 v120, v38, v39
	v_cvt_pk_bf16_f32 v121, v42, v43
	s_waitcnt vmcnt(0)
	v_sub_u32_e32 v2, v153, v2
	v_and_b32_e32 v156, 4, v3
	v_and_b32_e32 v157, 48, v4
	s_sub_i32 s0, 0, s1
	s_sub_i32 s1, s87, s1
	s_mov_b32 m0, s81
	s_add_i32 s82, s87, 0x8400
	v_or3_b32 v3, v155, v154, v156
	v_lshl_or_b32 v2, v2, 6, v157
	s_mov_b32 m0, s82
	s_add_u32 s40, s20, 0x3000
	v_lshl_add_u32 v2, v3, 7, v2
	s_mov_b32 m0, s1
	s_addc_u32 s41, s21, 0
	s_add_i32 s83, s87, 0xc000
	s_mov_b32 m0, s83
	s_add_i32 s84, s87, 0xc400
	v_mov_b32_e32 v3, v1
	s_mov_b32 m0, s84
	v_lshl_add_u64 v[124:125], s[22:23], 0, v[2:3]
	s_mov_b64 s[40:41], 0x2000
	s_add_i32 m0, s1, 0x2000
	v_lshl_add_u64 v[2:3], v[124:125], 0, s[40:41]
	s_add_u32 s40, s20, 0x6000
	s_addc_u32 s41, s21, 0
	s_add_i32 m0, s87, 0x10000
	s_waitcnt vmcnt(3)
	s_waitcnt vmcnt(0) lgkmcnt(0)
	s_barrier
	global_load_lds_dwordx4 v0, s[40:41]
	s_add_i32 m0, s87, 0x10400
	v_lshlrev_b32_e32 v35, 8, v55
	global_load_lds_dwordx4 v122, s[40:41]
	s_mov_b64 s[40:41], 0x4000
	v_lshl_add_u64 v[2:3], v[124:125], 0, s[40:41]
	s_add_i32 m0, s1, 0x4000
	v_or_b32_e32 v38, 32, v34
	global_load_lds_dwordx4 v[2:3], off
	v_lshlrev_b32_e32 v2, 4, v55
	v_and_b32_e32 v37, 0x70, v2
	v_bitop3_b32 v140, v34, v35, v37 bitop3:0xde
	v_add_u32_e32 v126, 0, v140
	ds_read_b128 v[2:5], v126 offset:32768
	v_bitop3_b32 v141, v38, v35, v37 bitop3:0xde
	v_add_u32_e32 v127, 0, v141
	ds_read_b128 v[38:41], v127 offset:32768
	s_waitcnt lgkmcnt(0)
	v_mfma_f32_32x32x16_bf16 v[18:33], v[2:5], v[98:101], 0
	ds_read_b128 v[2:5], v126 offset:40960
	s_cmp_lt_i32 s38, 4
	v_mfma_f32_32x32x16_bf16 v[18:33], v[38:41], v[102:105], v[18:33]
	ds_read_b128 v[38:41], v127 offset:40960
	s_waitcnt lgkmcnt(0)
	v_mfma_f32_32x32x16_bf16 v[2:17], v[2:5], v[98:101], 0
	v_mfma_f32_32x32x16_bf16 v[2:17], v[38:41], v[102:105], v[2:17]
	v_or_b32_e32 v38, 64, v34
	v_bitop3_b32 v142, v38, v35, v37 bitop3:0xde
	v_add_u32_e32 v128, 0, v142
	ds_read_b128 v[38:41], v128 offset:32768
	s_waitcnt lgkmcnt(0)
	v_mfma_f32_32x32x16_bf16 v[18:33], v[38:41], v[106:109], v[18:33]
	ds_read_b128 v[38:41], v128 offset:40960
	s_waitcnt lgkmcnt(0)
	v_mfma_f32_32x32x16_bf16 v[2:17], v[38:41], v[106:109], v[2:17]
	v_or_b32_e32 v38, 0x60, v34
	v_bitop3_b32 v143, v38, v35, v37 bitop3:0xde
	v_add_u32_e32 v129, 0, v143
	ds_read_b128 v[38:41], v129 offset:32768
	s_waitcnt lgkmcnt(0)
	v_mfma_f32_32x32x16_bf16 v[18:33], v[38:41], v[110:113], v[18:33]
	ds_read_b128 v[38:41], v129 offset:40960
	s_waitcnt lgkmcnt(0)
	v_mfma_f32_32x32x16_bf16 v[2:17], v[38:41], v[110:113], v[2:17]
	v_or_b32_e32 v38, 0x80, v34
	v_bitop3_b32 v144, v38, v35, v37 bitop3:0xde
	v_add_u32_e32 v130, 0, v144
	ds_read_b128 v[38:41], v130 offset:32768
	v_or_b32_e32 v34, 0xa0, v34
	v_bitop3_b32 v145, v34, v35, v37 bitop3:0xde
	v_add_u32_e32 v131, 0, v145
	s_waitcnt lgkmcnt(0)
	v_mfma_f32_32x32x16_bf16 v[18:33], v[38:41], v[114:117], v[18:33]
	ds_read_b128 v[38:41], v130 offset:40960
	s_waitcnt lgkmcnt(0)
	v_mfma_f32_32x32x16_bf16 v[2:17], v[38:41], v[114:117], v[2:17]
	ds_read_b128 v[38:41], v131 offset:32768
	s_waitcnt lgkmcnt(0)
	v_mfma_f32_32x32x16_bf16 v[18:33], v[38:41], v[118:121], v[18:33]
	ds_read_b128 v[38:41], v131 offset:40960
	s_waitcnt lgkmcnt(0)
	v_mfma_f32_32x32x16_bf16 v[2:17], v[38:41], v[118:121], v[2:17]
	s_cbranch_scc1 .LBB0_1417
	s_setprio 1
